# baseline (speedup 1.0000x reference)
.Lchain_top:
.Lit_A:
	v_add_u32_sdwa v88, v116, v42 dst_sel:DWORD dst_unused:UNUSED_PAD src0_sel:DWORD src1_sel:WORD_0
	v_add_u32_sdwa v89, v116, v42 dst_sel:DWORD dst_unused:UNUSED_PAD src0_sel:DWORD src1_sel:WORD_1
	ds_read_b64 v[68:69], v88
	v_add_u32_sdwa v90, v116, v43 dst_sel:DWORD dst_unused:UNUSED_PAD src0_sel:DWORD src1_sel:WORD_0
	ds_read_b64 v[70:71], v89
	v_add_u32_sdwa v91, v116, v43 dst_sel:DWORD dst_unused:UNUSED_PAD src0_sel:DWORD src1_sel:WORD_1
	ds_read_b64 v[72:73], v90
	ds_read_b64 v[74:75], v91
	v_add_u32_sdwa v92, v105, v52 dst_sel:DWORD dst_unused:UNUSED_PAD src0_sel:DWORD src1_sel:WORD_0
	v_add_u32_sdwa v93, v105, v52 dst_sel:DWORD dst_unused:UNUSED_PAD src0_sel:DWORD src1_sel:WORD_1
	v_add_u32_sdwa v106, v105, v53 dst_sel:DWORD dst_unused:UNUSED_PAD src0_sel:DWORD src1_sel:WORD_0
	v_add_u32_sdwa v107, v105, v53 dst_sel:DWORD dst_unused:UNUSED_PAD src0_sel:DWORD src1_sel:WORD_1
	v_add_u32_sdwa v108, v105, v54 dst_sel:DWORD dst_unused:UNUSED_PAD src0_sel:DWORD src1_sel:WORD_0
	v_add_u32_sdwa v109, v105, v54 dst_sel:DWORD dst_unused:UNUSED_PAD src0_sel:DWORD src1_sel:WORD_1
	v_add_u32_sdwa v88, v105, v55 dst_sel:DWORD dst_unused:UNUSED_PAD src0_sel:DWORD src1_sel:WORD_0
	v_add_u32_sdwa v89, v105, v55 dst_sel:DWORD dst_unused:UNUSED_PAD src0_sel:DWORD src1_sel:WORD_1
	ds_read_b128 v[120:123], v92
	ds_read_b128 v[124:127], v93
	ds_read_b128 v[128:131], v106
	ds_read_b128 v[132:135], v107
	ds_read_b128 v[140:143], v108
	ds_read_b128 v[144:147], v109
	ds_read_b128 v[148:151], v88
	ds_read_b128 v[152:155], v89
	v_add_u32_sdwa v118, v116, v39 dst_sel:DWORD dst_unused:UNUSED_PAD src0_sel:DWORD src1_sel:WORD_0
	v_add_u32_sdwa v119, v116, v39 dst_sel:DWORD dst_unused:UNUSED_PAD src0_sel:DWORD src1_sel:WORD_1
	v_add_u32_sdwa v136, v116, v41 dst_sel:DWORD dst_unused:UNUSED_PAD src0_sel:DWORD src1_sel:WORD_0
	s_waitcnt lgkmcnt(11)
	v_pk_add_f32 v[76:77], v[44:45], v[68:69]
	s_waitcnt lgkmcnt(9)
	v_pk_add_f32 v[78:79], v[70:71], v[72:73]
	s_waitcnt lgkmcnt(8)
	v_pk_add_f32 v[76:77], v[76:77], v[74:75]
	s_nop 0
	v_pk_add_f32 v[76:77], v[76:77], v[78:79]
	s_bitcmp1_b32 s4, 10
	s_cbranch_scc1 .Lnearslow_A
.Lnearslow_ret_A:
	v_pk_mul_f32 v[78:79], v[40:41], v[76:77] op_sel_hi:[0,1]
	ds_write_b64 v137, v[78:79]
	ds_read_b128 v[46:49], v138 offset:57408
	ds_read_b64 v[50:51], v139
	ds_read2_b64 v[56:59], v156 offset1:2
	ds_read2_b32 v[60:61], v157 offset1:16
	s_and_b32 s9, s4, 0xff
	s_waitcnt lgkmcnt(4)
	s_bitcmp1_b32 s4, 9
	s_cbranch_scc1 .Lfs_A
	s_cmp_eq_u32 s9, 0
	s_cbranch_scc1 .Lfs_A
	ds_read_b64 v[82:83], v118
	ds_read_b64 v[84:85], v119
	ds_read_b64 v[86:87], v136

.Lfarslow_ret_A:
	v_pk_add_f32 v[120:121], v[120:121], v[128:129]
	v_pk_add_f32 v[122:123], v[122:123], v[130:131]
	v_pk_add_f32 v[140:141], v[140:141], v[148:149]
	v_pk_add_f32 v[142:143], v[142:143], v[150:151]
	v_pk_add_f32 v[120:121], v[120:121], v[140:141]
	v_pk_add_f32 v[122:123], v[122:123], v[142:143]
	s_nop 1
	v_permlane32_swap_b32_e32 v120, v122
	v_permlane32_swap_b32_e32 v121, v123
	v_pk_add_f32 v[62:63], v[120:121], v[122:123]
	s_bitcmp1_b32 s4, 9
	s_cbranch_scc1 .Lslowlev_A
	s_cmp_eq_u32 s9, 0
	s_cbranch_scc1 .Llevdone_A
	s_waitcnt lgkmcnt(2)
	v_pk_fma_f32 v[80:81], v[40:41], v[82:83], v[78:79] op_sel_hi:[0,1,1]
	s_waitcnt lgkmcnt(1)
	v_pk_fma_f32 v[80:81], v[40:41], v[84:85], v[80:81] op_sel_hi:[0,1,1]
	s_waitcnt lgkmcnt(0)
	v_pk_fma_f32 v[80:81], v[40:41], v[86:87], v[80:81] op_sel_hi:[0,1,1]
	ds_write_b64 v137, v[80:81]
	s_cmp_lt_u32 s9, 2
	s_cbranch_scc1 .Llevdone_A
	s_sub_u32 s8, s9, 1
.Llev_A:
	ds_read_b64 v[82:83], v118
	ds_read_b64 v[84:85], v119
	ds_read_b64 v[86:87], v136
	s_sub_u32 s8, s8, 1
	s_waitcnt lgkmcnt(2)
	v_pk_fma_f32 v[80:81], v[40:41], v[82:83], v[78:79] op_sel_hi:[0,1,1]
	s_waitcnt lgkmcnt(1)
	v_pk_fma_f32 v[80:81], v[40:41], v[84:85], v[80:81] op_sel_hi:[0,1,1]
	s_waitcnt lgkmcnt(0)
	v_pk_fma_f32 v[80:81], v[40:41], v[86:87], v[80:81] op_sel_hi:[0,1,1]
	ds_write_b64 v137, v[80:81]
	s_cmp_lg_u32 s8, 0
	s_cbranch_scc1 .Llev_A

.Lit_B:
	v_add_u32_sdwa v88, v116, v50 dst_sel:DWORD dst_unused:UNUSED_PAD src0_sel:DWORD src1_sel:WORD_0
	v_add_u32_sdwa v89, v116, v50 dst_sel:DWORD dst_unused:UNUSED_PAD src0_sel:DWORD src1_sel:WORD_1
	ds_read_b64 v[68:69], v88
	v_add_u32_sdwa v90, v116, v51 dst_sel:DWORD dst_unused:UNUSED_PAD src0_sel:DWORD src1_sel:WORD_0
	ds_read_b64 v[70:71], v89
	v_add_u32_sdwa v91, v116, v51 dst_sel:DWORD dst_unused:UNUSED_PAD src0_sel:DWORD src1_sel:WORD_1
	ds_read_b64 v[72:73], v90
	ds_read_b64 v[74:75], v91
	v_add_u32_sdwa v92, v105, v56 dst_sel:DWORD dst_unused:UNUSED_PAD src0_sel:DWORD src1_sel:WORD_0
	v_add_u32_sdwa v93, v105, v56 dst_sel:DWORD dst_unused:UNUSED_PAD src0_sel:DWORD src1_sel:WORD_1
	v_add_u32_sdwa v106, v105, v57 dst_sel:DWORD dst_unused:UNUSED_PAD src0_sel:DWORD src1_sel:WORD_0
	v_add_u32_sdwa v107, v105, v57 dst_sel:DWORD dst_unused:UNUSED_PAD src0_sel:DWORD src1_sel:WORD_1
	v_add_u32_sdwa v108, v105, v58 dst_sel:DWORD dst_unused:UNUSED_PAD src0_sel:DWORD src1_sel:WORD_0
	v_add_u32_sdwa v109, v105, v58 dst_sel:DWORD dst_unused:UNUSED_PAD src0_sel:DWORD src1_sel:WORD_1
	v_add_u32_sdwa v88, v105, v59 dst_sel:DWORD dst_unused:UNUSED_PAD src0_sel:DWORD src1_sel:WORD_0
	v_add_u32_sdwa v89, v105, v59 dst_sel:DWORD dst_unused:UNUSED_PAD src0_sel:DWORD src1_sel:WORD_1
	ds_read_b128 v[120:123], v92
	ds_read_b128 v[124:127], v93
	ds_read_b128 v[128:131], v106
	ds_read_b128 v[132:135], v107
	ds_read_b128 v[140:143], v108
	ds_read_b128 v[144:147], v109
	ds_read_b128 v[148:151], v88
	ds_read_b128 v[152:155], v89
	v_add_u32_sdwa v118, v116, v47 dst_sel:DWORD dst_unused:UNUSED_PAD src0_sel:DWORD src1_sel:WORD_0
	v_add_u32_sdwa v119, v116, v47 dst_sel:DWORD dst_unused:UNUSED_PAD src0_sel:DWORD src1_sel:WORD_1
	v_add_u32_sdwa v136, v116, v49 dst_sel:DWORD dst_unused:UNUSED_PAD src0_sel:DWORD src1_sel:WORD_0
	s_waitcnt lgkmcnt(11)
	v_pk_add_f32 v[76:77], v[62:63], v[68:69]
	s_waitcnt lgkmcnt(9)
	v_pk_add_f32 v[78:79], v[70:71], v[72:73]
	s_waitcnt lgkmcnt(8)
	v_pk_add_f32 v[76:77], v[76:77], v[74:75]
	s_nop 0
	v_pk_add_f32 v[76:77], v[76:77], v[78:79]
	s_bitcmp1_b32 s21, 10
	s_cbranch_scc1 .Lnearslow_B
.Lnearslow_ret_B:
	v_pk_mul_f32 v[78:79], v[48:49], v[76:77] op_sel_hi:[0,1]
	ds_write_b64 v137, v[78:79]
	ds_read_b128 v[38:41], v138 offset:57408
	ds_read_b64 v[42:43], v139
	ds_read2_b64 v[52:55], v156 offset1:2
	ds_read2_b32 v[60:61], v157 offset1:16
	s_and_b32 s9, s21, 0xff
	s_waitcnt lgkmcnt(4)
	s_bitcmp1_b32 s21, 9
	s_cbranch_scc1 .Lfs_B
	s_cmp_eq_u32 s9, 0
	s_cbranch_scc1 .Lfs_B
	ds_read_b64 v[82:83], v118
	ds_read_b64 v[84:85], v119
	ds_read_b64 v[86:87], v136

.Lfarslow_ret_B:
	v_pk_add_f32 v[120:121], v[120:121], v[128:129]
	v_pk_add_f32 v[122:123], v[122:123], v[130:131]
	v_pk_add_f32 v[140:141], v[140:141], v[148:149]
	v_pk_add_f32 v[142:143], v[142:143], v[150:151]
	v_pk_add_f32 v[120:121], v[120:121], v[140:141]
	v_pk_add_f32 v[122:123], v[122:123], v[142:143]
	s_nop 1
	v_permlane32_swap_b32_e32 v120, v122
	v_permlane32_swap_b32_e32 v121, v123
	v_pk_add_f32 v[44:45], v[120:121], v[122:123]
	s_bitcmp1_b32 s21, 9
	s_cbranch_scc1 .Lslowlev_B
	s_cmp_eq_u32 s9, 0
	s_cbranch_scc1 .Llevdone_B
	s_waitcnt lgkmcnt(2)
	v_pk_fma_f32 v[80:81], v[48:49], v[82:83], v[78:79] op_sel_hi:[0,1,1]
	s_waitcnt lgkmcnt(1)
	v_pk_fma_f32 v[80:81], v[48:49], v[84:85], v[80:81] op_sel_hi:[0,1,1]
	s_waitcnt lgkmcnt(0)
	v_pk_fma_f32 v[80:81], v[48:49], v[86:87], v[80:81] op_sel_hi:[0,1,1]
	ds_write_b64 v137, v[80:81]
	s_cmp_lt_u32 s9, 2
	s_cbranch_scc1 .Llevdone_B
	s_sub_u32 s8, s9, 1
.Llev_B:
	ds_read_b64 v[82:83], v118
	ds_read_b64 v[84:85], v119
	ds_read_b64 v[86:87], v136
	s_sub_u32 s8, s8, 1
	s_waitcnt lgkmcnt(2)
	v_pk_fma_f32 v[80:81], v[48:49], v[82:83], v[78:79] op_sel_hi:[0,1,1]
	s_waitcnt lgkmcnt(1)
	v_pk_fma_f32 v[80:81], v[48:49], v[84:85], v[80:81] op_sel_hi:[0,1,1]
	s_waitcnt lgkmcnt(0)
	v_pk_fma_f32 v[80:81], v[48:49], v[86:87], v[80:81] op_sel_hi:[0,1,1]
	ds_write_b64 v137, v[80:81]
	s_cmp_lg_u32 s8, 0
	s_cbranch_scc1 .Llev_B

.Lsl_A:
	s_add_u32 s8, s8, 1
	ds_read_b64 v[82:83], v118
	ds_read_b64 v[84:85], v119
	ds_read_b64 v[86:87], v136
	s_waitcnt lgkmcnt(2)
	v_pk_fma_f32 v[80:81], v[40:41], v[82:83], v[78:79] op_sel_hi:[0,1,1]
	s_waitcnt lgkmcnt(1)
	v_pk_fma_f32 v[80:81], v[40:41], v[84:85], v[80:81] op_sel_hi:[0,1,1]
	s_waitcnt lgkmcnt(0)
	v_pk_fma_f32 v[80:81], v[40:41], v[86:87], v[80:81] op_sel_hi:[0,1,1]
	v_cmp_ne_u32_e32 vcc, 0, v165
	s_and_saveexec_b64 s[12:13], vcc
	s_cbranch_execz .Lsl_w_A
	ds_read_b32 v167, v164
	s_waitcnt lgkmcnt(0)

.Lsl_w_A:
	s_mov_b64 exec, -1
	ds_write_b64 v137, v[80:81]
	s_cmp_le_u32 s8, s9
	s_cbranch_scc1 .Lsl_A
	s_branch .Llevdone_A

.Lsl_B:
	s_add_u32 s8, s8, 1
	ds_read_b64 v[82:83], v118
	ds_read_b64 v[84:85], v119
	ds_read_b64 v[86:87], v136
	s_waitcnt lgkmcnt(2)
	v_pk_fma_f32 v[80:81], v[48:49], v[82:83], v[78:79] op_sel_hi:[0,1,1]
	s_waitcnt lgkmcnt(1)
	v_pk_fma_f32 v[80:81], v[48:49], v[84:85], v[80:81] op_sel_hi:[0,1,1]
	s_waitcnt lgkmcnt(0)
	v_pk_fma_f32 v[80:81], v[48:49], v[86:87], v[80:81] op_sel_hi:[0,1,1]
	v_cmp_ne_u32_e32 vcc, 0, v165
	s_and_saveexec_b64 s[12:13], vcc
	s_cbranch_execz .Lsl_w_B
	ds_read_b32 v167, v164
	s_waitcnt lgkmcnt(0)
